# v_all with conversion re-split 2: P4 converts W1 items 2048..6143, P2 converts 6144..24575 (all W2 incl. experts>=24), P9 converts nothing
# baseline (speedup 1.0000x reference)
; #define LAS __attribute__((address_space(3)))
; __device__ __forceinline__ void cvt_fill_g(const Frame& F) { LAS float* gl = (LAS float*)(F.lds + BG_G_OFF); for (int i = F.tid; i < DM; i += NTHREADS) gl[i] = F.g_moe[i] * WSCALE; __syncthreads(); }
;     __device__ __forceinline__ void init(const Frame& F_, int first_item, int n_items) { init(F_, first_item, n_items, F_.vcu, F_.G); }
; __global__ void __launch_bounds__(NTHREADS, 2) mk_fwd(Args args) {
;     ...
;         cvt_fill_g(F);
;         Bg bg; bg.init(F, CVT_P0_ITEMS, CVT_ITEMS - CVT_P0_ITEMS - (F.G == 256 ? CVT_P9_ITEMS + CVT_P4_ITEMS + CVT_P1_ITEMS : 0));
.LBB0_367:
	global_load_dword v5, v[2:3], off
	v_add_u32_e32 v4, 0x200, v4
	v_cmp_lt_u32_e32 vcc, s3, v4
	v_lshl_add_u64 v[2:3], v[2:3], 0, s[4:5]
	s_or_b64 s[0:1], vcc, s[0:1]
	s_waitcnt vmcnt(0)
	v_mul_f32_e32 v5, 0x42800000, v5
	ds_write_b32 v1, v5
	v_add_u32_e32 v1, 0x800, v1
	s_andn2_b64 exec, exec, s[0:1]
	s_cbranch_execnz .LBB0_367
	s_or_b64 exec, exec, s[0:1]
	s_cmpk_eq_i32 s33, 0x100
	s_movk_i32 s0, 0x6000
	v_readlane_b32 s1, v254, 8
	s_cselect_b32 s0, s0, 0x6000
	s_lshl_b32 s3, s52, 2
	s_lshr_b32 s1, s1, 7
	s_add_i32 s3, s3, s1
	s_addk_i32 s3, 0x1800
	s_lshl_b32 s55, s33, 2
	s_cmp_ge_i32 s3, s0
	s_mov_b32 s54, 0
	s_waitcnt lgkmcnt(0)
	s_barrier
	s_cbranch_scc1 .LBB0_370
	s_abs_i32 s1, s55
	v_cvt_f32_u32_e32 v1, s1
	s_add_i32 s0, s55, s0
	s_not_b32 s4, s3
	s_add_i32 s4, s4, s0
	v_rcp_iflag_f32_e32 v1, v1
	s_sub_i32 s0, 0, s1
	s_xor_b32 s5, s4, s55
	s_abs_i32 s4, s4
	v_mul_f32_e32 v1, 0x4f7ffffe, v1
	v_cvt_u32_f32_e32 v1, v1
	s_ashr_i32 s5, s5, 31
	v_readfirstlane_b32 s6, v1
	s_mul_i32 s0, s0, s6
	s_mul_hi_u32 s0, s6, s0
	s_add_i32 s6, s6, s0
	s_mul_hi_u32 s0, s4, s6
	s_mul_i32 s6, s0, s1
	s_sub_i32 s4, s4, s6
	s_add_i32 s7, s0, 1
	s_sub_i32 s6, s4, s1
	s_cmp_ge_u32 s4, s1
	s_cselect_b32 s0, s7, s0
	s_cselect_b32 s4, s6, s4
	s_add_i32 s6, s0, 1
	s_cmp_ge_u32 s4, s1
	s_cselect_b32 s0, s6, s0
	s_xor_b32 s0, s0, s5
	s_sub_i32 s0, s0, s5
	s_lshl_b32 s54, s0, 1

; #define LAS __attribute__((address_space(3)))
; __device__ __forceinline__ void cvt_fill_g(const Frame& F) { LAS float* gl = (LAS float*)(F.lds + BG_G_OFF); for (int i = F.tid; i < DM; i += NTHREADS) gl[i] = F.g_moe[i] * WSCALE; __syncthreads(); }
;     __device__ __forceinline__ void init(const Frame& F_, int first_item, int n_items) { init(F_, first_item, n_items, F_.vcu, F_.G); }
; __global__ void __launch_bounds__(NTHREADS, 2) mk_fwd(Args args) {
;     ...
;         if (F.G == 256 && blockIdx.x >= 128) {
;             cvt_fill_g(F);
;             Bg bg; bg.init(F, CVT_ITEMS - CVT_P9_ITEMS - CVT_P4_ITEMS, CVT_P4_ITEMS, (int)blockIdx.x - 128, 128); bg.drain();
.LBB0_892:
	global_load_dword v6, v[2:3], off
	v_add_u32_e32 v5, 0x200, v5
	v_cmp_lt_u32_e32 vcc, s3, v5
	v_lshl_add_u64 v[2:3], v[2:3], 0, s[4:5]
	s_or_b64 s[0:1], vcc, s[0:1]
	s_waitcnt vmcnt(0)
	v_mul_f32_e32 v6, 0x42800000, v6
	ds_write_b32 v4, v6
	v_add_u32_e32 v4, 0x800, v4
	s_andn2_b64 exec, exec, s[0:1]
	s_cbranch_execnz .LBB0_892
	s_or_b64 exec, exec, s[0:1]
	v_readlane_b32 s1, v254, 8
	s_lshl_b32 s0, s2, 2
	s_lshr_b32 s1, s1, 7
	s_add_i32 s3, s0, s1
	s_addk_i32 s3, 0x600
	s_cmpk_gt_i32 s3, 0x17ff
	s_mov_b32 s34, 0
	s_waitcnt lgkmcnt(0)
	s_barrier
	s_cbranch_scc1 .LBB0_895
	s_sub_i32 s0, 0x19ff, s3
	s_ashr_i32 s1, s0, 31
	s_lshr_b32 s1, s1, 23
	s_add_i32 s0, s0, s1
	s_ashr_i32 s0, s0, 9
	s_lshl_b32 s34, s0, 1

; #define LAS __attribute__((address_space(3)))
;     __device__ __forceinline__ void init(const Frame& F_, int first_item, int n_items) { init(F_, first_item, n_items, F_.vcu, F_.G); }
; __global__ void __launch_bounds__(NTHREADS, 2) mk_fwd(Args args) {
;     ...
;         moe_tables(F, 8);
;         const LAS int* tab = (const LAS int*)(lds + TAB_OFF);
;         SchedMoe<false> S{tab, F.G, F.vcu, (const char*)WSP(unsigned char, WS_H), (const char*)WSP(unsigned char, WS_W2), WSP(int, WS_ROWLIST), (size_t)DM * DE, 0, tab[32]};
;         EpiMlp2 E{tab, WSP(int, WS_ROWLIST), WSP(float, WS_ROWGATE), F.b_mlp2, WSP(unsigned char, WS_Y)};
;         const int total = tab[32], split = tab[CVT_P9_E0];
;         int nparts = 1, nconv = 0;
;         if (F.G == 256) {
;             const int rem = total & 255; int first = rem; nconv = 256 - rem;
;             if (nconv < 64) { first = 0; nconv = 256; }
;             nparts = 2;
;             if (F.vcu >= first) {
;                 Bg bg; bg.init(F, CVT_ITEMS - CVT_P9_ITEMS, CVT_P9_ITEMS, F.vcu - first, nconv); bg.drain();
.LBB0_1271:
	s_add_i32 s0, 0, 0x27880
	v_mov_b32_e32 v1, s0
	s_add_i32 s0, 0, 0x27860
	s_waitcnt vmcnt(0)
	v_mov_b32_e32 v2, s0
	s_waitcnt lgkmcnt(0)
	s_barrier
	ds_read_b32 v1, v1
	ds_read_b32 v2, v2
	s_cmpk_eq_i32 s33, 0x100
	s_mov_b32 s21, 0
	s_mov_b32 s54, 1
	s_waitcnt lgkmcnt(1)
	v_readfirstlane_b32 s34, v1
	s_waitcnt lgkmcnt(0)
	v_readfirstlane_b32 s35, v2
	s_cselect_b64 s[2:3], -1, 0
	s_cmpk_lg_i32 s33, 0x100
	s_mov_b32 s53, 0
	s_cbranch_scc1 .LBB0_1293
	s_and_b32 s0, s34, 0xff
	s_sub_i32 s1, 0x100, s0
	s_cmpk_gt_u32 s0, 0xc0
	s_cselect_b32 s4, 0, s0
	s_cselect_b32 s53, 0x100, s1
	s_cmp_lt_i32 s52, s4
	s_mov_b32 s12, 0
	s_cbranch_scc1 .LBB0_1292
	s_sub_i32 s0, s52, s4
	s_lshl_b32 s0, s0, 2
	s_lshr_b32 s5, s5, 7
	s_add_i32 s10, s5, s0
	s_addk_i32 s10, 0x5800
	s_lshl_b32 s11, s53, 2
	s_cmpk_gt_u32 s10, 0x57ff
	s_cbranch_scc1 .LBB0_1275
	v_cvt_f32_u32_e32 v1, s11
	s_sub_i32 s0, s11, s10
	s_addk_i32 s0, 0x5fff
	v_cvt_f32_u32_e32 v2, s0
	v_rcp_iflag_f32_e32 v3, v1
	s_nop 0
	v_mul_f32_e32 v3, v2, v3
	v_trunc_f32_e32 v3, v3
	v_cvt_u32_f32_e32 v4, v3
	v_fma_f32 v2, -v3, v1, v2
	v_cmp_ge_f32_e64 s[0:1], |v2|, v1
	s_cmp_lg_u64 s[0:1], 0
	v_readfirstlane_b32 s8, v4
	s_addc_u32 s0, s8, 0
	s_and_b32 s0, s0, 0xffff
	s_lshl_b32 s12, s0, 1
